# v52 + nt cache policy on k_agg1g2 single-use list loads (keep Y gather set in L2)
# baseline (speedup 1.0000x reference)
.LBB2_4:
	v_lshl_or_b32 v60, s33, 17, v111
	s_lshl_b32 s42, s33, 6
	v_lshl_add_u64 v[80:81], v[60:61], 4, v[62:63]
	v_or_b32_e32 v60, s42, v59
	v_lshl_add_u64 v[10:11], v[60:61], 2, s[24:25]
	global_load_dwordx4 v[2:5], v[10:11], off offset:16 nt
	global_load_dwordx4 v[6:9], v[10:11], off nt
	v_mov_b32_e32 v88, 0
	v_mov_b32_e32 v89, 0
	v_mov_b32_e32 v86, 0
	v_mov_b32_e32 v87, 0
	v_mov_b32_e32 v84, 0
	v_mov_b32_e32 v85, 0
	v_mov_b32_e32 v82, 0
	v_mov_b32_e32 v83, 0
	s_and_saveexec_b64 s[10:11], s[28:29]
	s_cbranch_execz .LBB2_6
	v_lshl_add_u64 v[10:11], v[80:81], 0, v[64:65]
	s_waitcnt lgkmcnt(6)
	global_load_dwordx4 v[10:13], v[10:11], off
	s_waitcnt vmcnt(0)
	v_cvt_f32_f16_e32 v14, v10
	v_cvt_f32_f16_e32 v16, v11
	v_cvt_f32_f16_e32 v18, v12
	v_cvt_f32_f16_e32 v20, v13
	s_waitcnt lgkmcnt(2)
	v_cvt_f32_f16_sdwa v21, v13 dst_sel:DWORD dst_unused:UNUSED_PAD src0_sel:WORD_1
	v_cvt_f32_f16_sdwa v19, v12 dst_sel:DWORD dst_unused:UNUSED_PAD src0_sel:WORD_1
	v_cvt_f32_f16_sdwa v17, v11 dst_sel:DWORD dst_unused:UNUSED_PAD src0_sel:WORD_1
	v_cvt_f32_f16_sdwa v15, v10 dst_sel:DWORD dst_unused:UNUSED_PAD src0_sel:WORD_1
	v_pk_fma_f32 v[82:83], v[72:73], v[20:21], 0 op_sel_hi:[1,1,0]
	v_pk_fma_f32 v[84:85], v[70:71], v[18:19], 0 op_sel_hi:[1,1,0]
	v_pk_fma_f32 v[86:87], v[68:69], v[16:17], 0 op_sel_hi:[1,1,0]
	v_pk_fma_f32 v[88:89], v[56:57], v[14:15], 0 op_sel_hi:[1,1,0]
